# v39 + indexer ticket drawn one unit ahead and wave 0 head wait counted (vmcnt 16) so it no longer waits for the bitmask store acks
# baseline (speedup 1.0000x reference)
.LBB0_1231:
	s_waitcnt lgkmcnt(1)
	v_mov_b32_e32 v0, 0
	s_and_saveexec_b64 s[40:41], s[36:37]
	s_cbranch_execz .LBB0_1235
	s_waitcnt vmcnt(16) lgkmcnt(0)
	v_mov_b32_e32 v0, v229
